# baseline (speedup 1.0000x reference)
.LBB2_101:
	s_or_b64 exec, exec, s[40:41]
	s_setprio 3
	s_mov_b64 s[2:3], s[56:57]
	s_mov_b64 s[4:5], s[58:59]
	s_mov_b64 s[6:7], s[60:61]
	v_lshlrev_b32_e32 v132, 15, v66
	v_mov_b32_e32 v133, 0
	s_waitcnt lgkmcnt(0)
	v_lshl_add_u64 v[26:27], s[6:7], 0, v[132:133]
	v_lshlrev_b32_e32 v132, 4, v146
	v_lshl_add_u64 v[66:67], v[26:27], 0, v[132:133]
	s_movk_i32 s9, 0x1000
	v_add_co_u32_e32 v68, vcc, s9, v66
	s_movk_i32 s11, 0x2000
	s_nop 0
	v_addc_co_u32_e32 v69, vcc, 0, v67, vcc
	v_add_co_u32_e32 v70, vcc, s11, v66
	global_load_dwordx4 v[86:89], v[66:67], off
	s_nop 0
	v_addc_co_u32_e32 v71, vcc, 0, v67, vcc
	global_load_dwordx4 v[90:93], v[70:71], off offset:-4096
	s_movk_i32 s12, 0x3000
	v_add_co_u32_e32 v72, vcc, s12, v66
	s_movk_i32 s8, 0x4000
	s_nop 0
	v_addc_co_u32_e32 v73, vcc, 0, v67, vcc
	v_add_co_u32_e32 v74, vcc, s8, v66
	global_load_dwordx4 v[94:97], v[70:71], off
	s_waitcnt vmcnt(4)
	v_addc_co_u32_e32 v75, vcc, 0, v67, vcc
	global_load_dwordx4 v[98:101], v[74:75], off offset:-4096
	s_movk_i32 s10, 0x5000
	v_add_co_u32_e32 v76, vcc, s10, v66
	s_movk_i32 s7, 0x6000
	s_nop 0
	v_addc_co_u32_e32 v77, vcc, 0, v67, vcc
	v_add_co_u32_e32 v78, vcc, s7, v66
	global_load_dwordx4 v[102:105], v[74:75], off
	s_nop 0
	v_addc_co_u32_e32 v79, vcc, 0, v67, vcc
	global_load_dwordx4 v[110:113], v[78:79], off
	global_load_dwordx4 v[106:109], v[78:79], off offset:-4096
	s_movk_i32 s6, 0x7000
	v_add_co_u32_e32 v80, vcc, s6, v66
	s_movk_i32 s0, 0x110
	s_nop 0
	v_addc_co_u32_e32 v81, vcc, 0, v67, vcc
	global_load_dwordx4 v[114:117], v[80:81], off
	global_load_dwordx4 v[58:61], v[66:67], off offset:1024
	global_load_dwordx4 v[62:65], v[68:69], off offset:1024
	global_load_dwordx4 v[54:57], v[70:71], off offset:1024
	global_load_dwordx4 v[50:53], v[72:73], off offset:1024
	global_load_dwordx4 v[46:49], v[74:75], off offset:1024
	global_load_dwordx4 v[42:45], v[76:77], off offset:1024
	global_load_dwordx4 v[34:37], v[78:79], off offset:1024
	global_load_dwordx4 v[26:29], v[80:81], off offset:1024
	v_mad_u32_u24 v85, v131, s0, v130
	v_add_u32_e32 v151, v85, v147
	ds_read_b128 v[38:41], v147 offset:17408
	s_waitcnt vmcnt(16)
	ds_read_b128 v[30:33], v147 offset:17472
	ds_read_b128 v[118:121], v151
	ds_read_b128 v[122:125], v151 offset:4352
	ds_read_b128 v[164:167], v151 offset:4416
	s_waitcnt vmcnt(15) lgkmcnt(2)
	v_mfma_f32_16x16x32_f16 v[126:129], v[86:89], v[118:121], v[38:41]
	s_waitcnt lgkmcnt(1)
	v_mfma_f32_16x16x32_f16 v[86:89], v[86:89], v[122:125], v[38:41]
	s_waitcnt vmcnt(14)
	v_mfma_f32_16x16x32_f16 v[134:137], v[90:93], v[118:121], v[30:33]
	v_mfma_f32_16x16x32_f16 v[90:93], v[90:93], v[122:125], v[30:33]
	global_load_dwordx4 v[38:41], v[66:67], off offset:2048
	s_nop 1
	global_load_dwordx4 v[30:33], v[68:69], off offset:2048
	ds_read_b128 v[22:25], v147 offset:17536
	ds_read_b128 v[18:21], v147 offset:17600
	s_waitcnt vmcnt(15) lgkmcnt(1)
	v_mfma_f32_16x16x32_f16 v[138:141], v[94:97], v[118:121], v[22:25]
	v_mfma_f32_16x16x32_f16 v[94:97], v[94:97], v[122:125], v[22:25]
	s_waitcnt vmcnt(14) lgkmcnt(0)
	v_mfma_f32_16x16x32_f16 v[142:145], v[98:101], v[118:121], v[18:21]
	v_mfma_f32_16x16x32_f16 v[98:101], v[98:101], v[122:125], v[18:21]
	global_load_dwordx4 v[22:25], v[70:71], off offset:2048
	s_nop 1
	global_load_dwordx4 v[18:21], v[72:73], off offset:2048
	ds_read_b128 v[6:9], v147 offset:17792
	s_waitcnt vmcnt(14) lgkmcnt(0)
	v_mfma_f32_16x16x32_f16 v[160:163], v[110:113], v[118:121], v[6:9]
	v_mfma_f32_16x16x32_f16 v[110:113], v[110:113], v[122:125], v[6:9]
	s_nop 2
	global_load_dwordx4 v[6:9], v[78:79], off offset:2048
	ds_read_b128 v[10:13], v147 offset:17728
	s_waitcnt vmcnt(14) lgkmcnt(0)
	v_mfma_f32_16x16x32_f16 v[156:159], v[106:109], v[118:121], v[10:13]
	v_mfma_f32_16x16x32_f16 v[106:109], v[106:109], v[122:125], v[10:13]
	s_nop 2
	global_load_dwordx4 v[10:13], v[76:77], off offset:2048
	ds_read_b128 v[14:17], v147 offset:17664
	s_waitcnt lgkmcnt(0)
	v_mfma_f32_16x16x32_f16 v[152:155], v[102:105], v[118:121], v[14:17]
	ds_read_b128 v[2:5], v147 offset:17856
	s_waitcnt vmcnt(14) lgkmcnt(0)
	v_mfma_f32_16x16x32_f16 v[118:121], v[114:117], v[118:121], v[2:5]
	v_mfma_f32_16x16x32_f16 v[114:117], v[114:117], v[122:125], v[2:5]
	s_nop 2
	global_load_dwordx4 v[2:5], v[80:81], off offset:2048
	v_mfma_f32_16x16x32_f16 v[102:105], v[102:105], v[122:125], v[14:17]
	ds_read_b128 v[122:125], v151 offset:64
	s_nop 1
	global_load_dwordx4 v[14:17], v[74:75], off offset:2048
	s_waitcnt vmcnt(15) lgkmcnt(0)
	v_mfma_f32_16x16x32_f16 v[126:129], v[58:61], v[122:125], v[126:129]
	v_mfma_f32_16x16x32_f16 v[58:61], v[58:61], v[164:167], v[86:89]
	s_waitcnt vmcnt(14)
	v_mfma_f32_16x16x32_f16 v[86:89], v[62:65], v[122:125], v[134:137]
	v_mfma_f32_16x16x32_f16 v[62:65], v[62:65], v[164:167], v[90:93]
	s_nop 1
	global_load_dwordx4 v[134:137], v[70:71], off offset:3072
	s_nop 0
	global_load_dwordx4 v[70:73], v[72:73], off offset:3072
	s_waitcnt vmcnt(15)
	v_mfma_f32_16x16x32_f16 v[90:93], v[54:57], v[122:125], v[138:141]
	v_mfma_f32_16x16x32_f16 v[54:57], v[54:57], v[164:167], v[94:97]
	s_nop 1
	global_load_dwordx4 v[138:141], v[74:75], off offset:3072
	s_nop 0
	global_load_dwordx4 v[74:77], v[76:77], off offset:3072
	s_waitcnt vmcnt(16)
	v_mfma_f32_16x16x32_f16 v[94:97], v[50:53], v[122:125], v[142:145]
	v_mfma_f32_16x16x32_f16 v[50:53], v[50:53], v[164:167], v[98:101]
	s_nop 1
	global_load_dwordx4 v[142:145], v[78:79], off offset:3072
	s_nop 0
	global_load_dwordx4 v[78:81], v[80:81], off offset:3072
	s_waitcnt vmcnt(17)
	v_mfma_f32_16x16x32_f16 v[98:101], v[46:49], v[122:125], v[152:155]
	v_mfma_f32_16x16x32_f16 v[46:49], v[46:49], v[164:167], v[102:105]
	s_waitcnt vmcnt(16)
	v_mfma_f32_16x16x32_f16 v[102:105], v[42:45], v[122:125], v[156:159]
	v_mfma_f32_16x16x32_f16 v[42:45], v[42:45], v[164:167], v[106:109]
	s_waitcnt vmcnt(15)
	v_mfma_f32_16x16x32_f16 v[106:109], v[34:37], v[122:125], v[160:163]
	v_mfma_f32_16x16x32_f16 v[34:37], v[34:37], v[164:167], v[110:113]
	s_waitcnt vmcnt(14)
	v_mfma_f32_16x16x32_f16 v[110:113], v[26:29], v[122:125], v[118:121]
	ds_read_b128 v[122:125], v151 offset:4480
	v_mfma_f32_16x16x32_f16 v[26:29], v[26:29], v[164:167], v[114:117]
	s_nop 0
	ds_read_b128 v[118:121], v151 offset:128
	s_nop 0
	global_load_dwordx4 v[114:117], v[66:67], off offset:3072
	s_nop 0
	global_load_dwordx4 v[66:69], v[68:69], off offset:3072
	s_waitcnt vmcnt(15) lgkmcnt(0)
	v_mfma_f32_16x16x32_f16 v[126:129], v[38:41], v[118:121], v[126:129]
	v_mfma_f32_16x16x32_f16 v[38:41], v[38:41], v[122:125], v[58:61]
	s_waitcnt vmcnt(14)
	v_mfma_f32_16x16x32_f16 v[58:61], v[30:33], v[118:121], v[86:89]
	s_waitcnt vmcnt(13)
	v_mfma_f32_16x16x32_f16 v[86:89], v[22:25], v[118:121], v[90:93]
	v_mfma_f32_16x16x32_f16 v[22:25], v[22:25], v[122:125], v[54:57]
	s_nop 1
	ds_read_b128 v[90:93], v151 offset:192
	s_waitcnt vmcnt(12)
	v_mfma_f32_16x16x32_f16 v[54:57], v[18:21], v[118:121], v[94:97]
	s_nop 2
	ds_read_b128 v[94:97], v151 offset:4544
	v_mfma_f32_16x16x32_f16 v[62:65], v[30:33], v[122:125], v[62:65]
	v_mfma_f32_16x16x32_f16 v[18:21], v[18:21], v[122:125], v[50:53]
	s_waitcnt vmcnt(8)
	v_mfma_f32_16x16x32_f16 v[50:53], v[14:17], v[118:121], v[98:101]
	v_mfma_f32_16x16x32_f16 v[14:17], v[14:17], v[122:125], v[46:49]
	v_mfma_f32_16x16x32_f16 v[46:49], v[10:13], v[118:121], v[102:105]
	v_mfma_f32_16x16x32_f16 v[10:13], v[10:13], v[122:125], v[42:45]
	v_mfma_f32_16x16x32_f16 v[42:45], v[6:9], v[118:121], v[106:109]
	v_mfma_f32_16x16x32_f16 v[6:9], v[6:9], v[122:125], v[34:37]
	v_mfma_f32_16x16x32_f16 v[34:37], v[2:5], v[118:121], v[110:113]
	v_mfma_f32_16x16x32_f16 v[2:5], v[2:5], v[122:125], v[26:29]
	s_waitcnt vmcnt(1) lgkmcnt(0)
	v_mfma_f32_16x16x32_f16 v[30:33], v[114:117], v[94:97], v[38:41]
	s_waitcnt vmcnt(0)
	v_mfma_f32_16x16x32_f16 v[26:29], v[66:69], v[94:97], v[62:65]
	v_mfma_f32_16x16x32_f16 v[22:25], v[134:137], v[94:97], v[22:25]
	v_mfma_f32_16x16x32_f16 v[18:21], v[70:73], v[94:97], v[18:21]
	v_mfma_f32_16x16x32_f16 v[14:17], v[138:141], v[94:97], v[14:17]
	v_mfma_f32_16x16x32_f16 v[10:13], v[74:77], v[94:97], v[10:13]
	v_mfma_f32_16x16x32_f16 v[6:9], v[142:145], v[94:97], v[6:9]
	v_mfma_f32_16x16x32_f16 v[2:5], v[78:81], v[94:97], v[2:5]
	v_mfma_f32_16x16x32_f16 v[126:129], v[114:117], v[90:93], v[126:129]
	v_mfma_f32_16x16x32_f16 v[122:125], v[66:69], v[90:93], v[58:61]
	v_mfma_f32_16x16x32_f16 v[118:121], v[134:137], v[90:93], v[86:89]
	v_mfma_f32_16x16x32_f16 v[114:117], v[70:73], v[90:93], v[54:57]
	v_mfma_f32_16x16x32_f16 v[106:109], v[138:141], v[90:93], v[50:53]
	v_mfma_f32_16x16x32_f16 v[110:113], v[74:77], v[90:93], v[46:49]
	v_mfma_f32_16x16x32_f16 v[102:105], v[142:145], v[90:93], v[42:45]
	v_mfma_f32_16x16x32_f16 v[98:101], v[78:81], v[90:93], v[34:37]
	s_nop 2
	v_xor_b32_e32 v34, 16, v83
	v_add_u32_e32 v35, 64, v84
	v_cmp_lt_i32_e32 vcc, v34, v35
	v_mov_b32_e32 v36, v127
	v_mov_b32_e32 v37, v123
	v_cndmask_b32_e32 v34, v83, v34, vcc
	v_lshlrev_b32_e32 v149, 2, v34
	v_xor_b32_e32 v34, 32, v83
	v_cmp_lt_i32_e32 vcc, v34, v35
	v_mov_b32_e32 v35, v122
	v_mov_b32_e32 v38, v129
	v_cndmask_b32_e32 v34, v83, v34, vcc
	v_lshlrev_b32_e32 v148, 2, v34
	v_mov_b32_e32 v34, v126
	v_pk_add_f32 v[34:35], v[34:35], v[36:37]
	v_mov_b32_e32 v36, v128
	v_mov_b32_e32 v37, v124
	v_mov_b32_e32 v39, v125
	v_pk_add_f32 v[36:37], v[36:37], v[38:39]
	v_mov_b32_e32 v38, v118
	v_pk_add_f32 v[34:35], v[34:35], v[36:37]
	v_mov_b32_e32 v36, v119
	v_mov_b32_e32 v37, v120
	v_mov_b32_e32 v39, v121
	v_pk_add_f32 v[36:37], v[36:37], v[38:39]
	v_add_f32_e32 v34, 0, v34
	v_pk_add_f32 v[36:37], v[36:37], v[36:37] op_sel:[0,1] op_sel_hi:[1,0]
	v_add_f32_e32 v34, v34, v35
	v_add_f32_e32 v38, v114, v115
	v_add_f32_e32 v40, v116, v117
	v_mov_b32_e32 v35, v106
	v_mov_b32_e32 v37, v107
	v_mov_b32_e32 v39, v108
	v_mov_b32_e32 v41, v109
	v_pk_add_f32 v[34:35], v[34:35], v[36:37]
	v_pk_add_f32 v[36:37], v[38:39], v[40:41]
	v_mov_b32_e32 v38, v110
	v_pk_add_f32 v[34:35], v[34:35], v[36:37]
	v_mov_b32_e32 v36, v111
	v_mov_b32_e32 v37, v112
	v_mov_b32_e32 v39, v113
	v_pk_add_f32 v[36:37], v[36:37], v[38:39]
	v_pk_add_f32 v[34:35], v[34:35], v[34:35] op_sel:[0,1] op_sel_hi:[1,0]
	v_pk_add_f32 v[36:37], v[36:37], v[36:37] op_sel:[0,1] op_sel_hi:[1,0]
	v_add_f32_e32 v38, v102, v103
	v_add_f32_e32 v40, v104, v105
	v_mov_b32_e32 v35, v98
	v_mov_b32_e32 v37, v99
	v_mov_b32_e32 v39, v100
	v_mov_b32_e32 v41, v101
	v_pk_add_f32 v[34:35], v[34:35], v[36:37]
	v_pk_add_f32 v[36:37], v[38:39], v[40:41]
	v_mov_b32_e32 v38, v31
	v_pk_add_f32 v[34:35], v[34:35], v[36:37]
	v_mov_b32_e32 v36, v30
	v_mov_b32_e32 v37, v26
	v_mov_b32_e32 v39, v27
	v_pk_add_f32 v[36:37], v[36:37], v[38:39]
	v_mov_b32_e32 v38, v32
	v_mov_b32_e32 v39, v28
	v_mov_b32_e32 v40, v33
	v_mov_b32_e32 v41, v29
	v_pk_add_f32 v[38:39], v[38:39], v[40:41]
	v_mov_b32_e32 v40, v22
	v_pk_add_f32 v[36:37], v[36:37], v[38:39]
	v_mov_b32_e32 v38, v23
	v_mov_b32_e32 v39, v24
	v_mov_b32_e32 v41, v25
	v_pk_add_f32 v[38:39], v[38:39], v[40:41]
	v_add_f32_e32 v36, 0, v36
	v_pk_add_f32 v[38:39], v[38:39], v[38:39] op_sel:[0,1] op_sel_hi:[1,0]
	v_add_f32_e32 v36, v36, v37
	v_add_f32_e32 v40, v18, v19
	v_add_f32_e32 v42, v20, v21
	v_mov_b32_e32 v37, v14
	v_mov_b32_e32 v39, v15
	v_mov_b32_e32 v41, v16
	v_mov_b32_e32 v43, v17
	v_pk_add_f32 v[36:37], v[36:37], v[38:39]
	v_pk_add_f32 v[38:39], v[40:41], v[42:43]
	v_mov_b32_e32 v40, v10
	v_pk_add_f32 v[36:37], v[36:37], v[38:39]
	v_mov_b32_e32 v38, v11
	v_mov_b32_e32 v39, v12
	v_mov_b32_e32 v41, v13
	v_pk_add_f32 v[38:39], v[38:39], v[40:41]
	v_pk_add_f32 v[36:37], v[36:37], v[36:37] op_sel:[0,1] op_sel_hi:[1,0]
	v_pk_add_f32 v[38:39], v[38:39], v[38:39] op_sel:[0,1] op_sel_hi:[1,0]
	v_add_f32_e32 v40, v6, v7
	v_add_f32_e32 v42, v8, v9
	v_mov_b32_e32 v37, v2
	v_mov_b32_e32 v39, v3
	v_mov_b32_e32 v41, v4
	v_mov_b32_e32 v43, v5
	v_pk_add_f32 v[36:37], v[36:37], v[38:39]
	v_pk_add_f32 v[38:39], v[40:41], v[42:43]
	s_brev_b32 s0, 60
	v_pk_add_f32 v[36:37], v[36:37], v[38:39]
	v_mov_b32_e32 v39, v34
	v_mov_b32_e32 v38, v36
	v_mov_b32_e32 v34, v37
	v_pk_add_f32 v[34:35], v[38:39], v[34:35]
	ds_bpermute_b32 v37, v149, v35
	ds_bpermute_b32 v36, v149, v34
	v_mov_b32_e32 v165, v126
	v_mov_b32_e32 v164, v30
	v_lshlrev_b32_e32 v150, 4, v82
	ds_read_b128 v[38:41], v150 offset:18880
	s_waitcnt lgkmcnt(1)
	v_pk_add_f32 v[134:135], v[34:35], v[36:37]
	ds_bpermute_b32 v137, v148, v135
	ds_bpermute_b32 v136, v148, v134
	ds_read_b128 v[34:37], v150 offset:18368
	ds_read_b128 v[42:45], v150 offset:18304
	ds_read_b128 v[46:49], v150 offset:18816
	ds_read_b128 v[90:93], v150 offset:17920
	s_waitcnt lgkmcnt(4)
	v_pk_add_f32 v[144:145], v[134:135], v[136:137]
	ds_read_b128 v[94:97], v150 offset:18432
	v_pk_mul_f32 v[134:135], v[144:145], s[0:1] op_sel_hi:[1,0]
	v_pk_fma_f32 v[164:165], v[144:145], s[0:1], v[164:165] op_sel_hi:[1,0,1] neg_lo:[1,0,0] neg_hi:[1,0,0]
	v_sub_f32_e32 v163, v126, v135
	v_mov_b32_e32 v126, v31
	v_sub_f32_e32 v162, v127, v135
	v_pk_fma_f32 v[126:127], v[144:145], s[0:1], v[126:127] op_sel_hi:[1,0,1] neg_lo:[1,0,0] neg_hi:[1,0,0]
	v_sub_f32_e32 v161, v128, v135
	v_pk_mul_f32 v[126:127], v[126:127], v[126:127]
	v_sub_f32_e32 v159, v122, v135
	v_pk_fma_f32 v[126:127], v[164:165], v[164:165], v[126:127]
	v_mov_b32_e32 v164, v32
	v_mov_b32_e32 v165, v128
	v_pk_fma_f32 v[164:165], v[144:145], s[0:1], v[164:165] op_sel_hi:[1,0,1] neg_lo:[1,0,0] neg_hi:[1,0,0]
	v_mov_b32_e32 v128, v33
	v_pk_fma_f32 v[126:127], v[164:165], v[164:165], v[126:127]
	v_pk_fma_f32 v[164:165], v[144:145], s[0:1], v[128:129] op_sel_hi:[1,0,1] neg_lo:[1,0,0] neg_hi:[1,0,0]
	v_sub_f32_e32 v158, v123, v135
	v_pk_fma_f32 v[126:127], v[164:165], v[164:165], v[126:127]
	v_mov_b32_e32 v164, v26
	v_mov_b32_e32 v165, v122
	v_pk_fma_f32 v[164:165], v[144:145], s[0:1], v[164:165] op_sel_hi:[1,0,1] neg_lo:[1,0,0] neg_hi:[1,0,0]
	v_mov_b32_e32 v122, v27
	v_pk_fma_f32 v[126:127], v[164:165], v[164:165], v[126:127]
	v_pk_fma_f32 v[122:123], v[144:145], s[0:1], v[122:123] op_sel_hi:[1,0,1] neg_lo:[1,0,0] neg_hi:[1,0,0]
	v_sub_f32_e32 v156, v124, v135
	v_pk_fma_f32 v[122:123], v[122:123], v[122:123], v[126:127]
	v_mov_b32_e32 v126, v28
	v_mov_b32_e32 v127, v124
	v_pk_fma_f32 v[126:127], v[144:145], s[0:1], v[126:127] op_sel_hi:[1,0,1] neg_lo:[1,0,0] neg_hi:[1,0,0]
	v_mov_b32_e32 v124, v29
	v_pk_fma_f32 v[122:123], v[126:127], v[126:127], v[122:123]
	v_pk_fma_f32 v[164:165], v[144:145], s[0:1], v[124:125] op_sel_hi:[1,0,1] neg_lo:[1,0,0] neg_hi:[1,0,0]
	v_sub_f32_e32 v153, v118, v135
	v_pk_fma_f32 v[122:123], v[164:165], v[164:165], v[122:123]
	v_mov_b32_e32 v164, v22
	v_mov_b32_e32 v165, v118
	v_pk_fma_f32 v[164:165], v[144:145], s[0:1], v[164:165] op_sel_hi:[1,0,1] neg_lo:[1,0,0] neg_hi:[1,0,0]
	v_mov_b32_e32 v118, v23
	v_sub_f32_e32 v157, v119, v135
	v_pk_fma_f32 v[122:123], v[164:165], v[164:165], v[122:123]
	v_pk_fma_f32 v[118:119], v[144:145], s[0:1], v[118:119] op_sel_hi:[1,0,1] neg_lo:[1,0,0] neg_hi:[1,0,0]
	v_sub_f32_e32 v155, v120, v135
	v_pk_fma_f32 v[118:119], v[118:119], v[118:119], v[122:123]
	v_mov_b32_e32 v122, v24
	v_mov_b32_e32 v123, v120
	v_pk_fma_f32 v[122:123], v[144:145], s[0:1], v[122:123] op_sel_hi:[1,0,1] neg_lo:[1,0,0] neg_hi:[1,0,0]
	v_mov_b32_e32 v120, v25
	v_sub_f32_e32 v160, v129, v135
	v_sub_f32_e32 v129, v121, v135
	v_pk_fma_f32 v[164:165], v[122:123], v[122:123], v[118:119]
	v_pk_fma_f32 v[120:121], v[144:145], s[0:1], v[120:121] op_sel_hi:[1,0,1] neg_lo:[1,0,0] neg_hi:[1,0,0]
	v_sub_f32_e32 v128, v114, v135
	v_pk_fma_f32 v[120:121], v[120:121], v[120:121], v[164:165]
	v_mov_b32_e32 v164, v18
	v_mov_b32_e32 v165, v114
	v_pk_fma_f32 v[164:165], v[144:145], s[0:1], v[164:165] op_sel_hi:[1,0,1] neg_lo:[1,0,0] neg_hi:[1,0,0]
	v_mov_b32_e32 v114, v19
	v_sub_f32_e32 v127, v115, v135
	v_pk_fma_f32 v[120:121], v[164:165], v[164:165], v[120:121]
	v_pk_fma_f32 v[114:115], v[144:145], s[0:1], v[114:115] op_sel_hi:[1,0,1] neg_lo:[1,0,0] neg_hi:[1,0,0]
	v_sub_f32_e32 v126, v116, v135
	v_pk_fma_f32 v[114:115], v[114:115], v[114:115], v[120:121]
	v_mov_b32_e32 v120, v20
	v_mov_b32_e32 v121, v116
	v_pk_fma_f32 v[120:121], v[144:145], s[0:1], v[120:121] op_sel_hi:[1,0,1] neg_lo:[1,0,0] neg_hi:[1,0,0]
	v_mov_b32_e32 v116, v21
	v_sub_f32_e32 v154, v125, v135
	v_sub_f32_e32 v125, v117, v135
	v_pk_fma_f32 v[114:115], v[120:121], v[120:121], v[114:115]
	v_pk_fma_f32 v[116:117], v[144:145], s[0:1], v[116:117] op_sel_hi:[1,0,1] neg_lo:[1,0,0] neg_hi:[1,0,0]
	v_sub_f32_e32 v124, v106, v135
	v_pk_fma_f32 v[114:115], v[116:117], v[116:117], v[114:115]
	v_mov_b32_e32 v116, v14
	v_mov_b32_e32 v117, v106
	v_pk_fma_f32 v[116:117], v[144:145], s[0:1], v[116:117] op_sel_hi:[1,0,1] neg_lo:[1,0,0] neg_hi:[1,0,0]
	v_mov_b32_e32 v106, v15
	v_sub_f32_e32 v123, v107, v135
	v_pk_fma_f32 v[114:115], v[116:117], v[116:117], v[114:115]
	v_pk_fma_f32 v[106:107], v[144:145], s[0:1], v[106:107] op_sel_hi:[1,0,1] neg_lo:[1,0,0] neg_hi:[1,0,0]
	v_sub_f32_e32 v122, v108, v135
	v_pk_fma_f32 v[106:107], v[106:107], v[106:107], v[114:115]
	v_mov_b32_e32 v114, v16
	v_mov_b32_e32 v115, v108
	v_pk_fma_f32 v[114:115], v[144:145], s[0:1], v[114:115] op_sel_hi:[1,0,1] neg_lo:[1,0,0] neg_hi:[1,0,0]
	v_mov_b32_e32 v108, v17
	v_pk_fma_f32 v[106:107], v[114:115], v[114:115], v[106:107]
	v_pk_fma_f32 v[114:115], v[144:145], s[0:1], v[108:109] op_sel_hi:[1,0,1] neg_lo:[1,0,0] neg_hi:[1,0,0]
	v_sub_f32_e32 v119, v110, v135
	v_pk_fma_f32 v[106:107], v[114:115], v[114:115], v[106:107]
	v_mov_b32_e32 v114, v10
	v_mov_b32_e32 v115, v110
	v_pk_fma_f32 v[114:115], v[144:145], s[0:1], v[114:115] op_sel_hi:[1,0,1] neg_lo:[1,0,0] neg_hi:[1,0,0]
	v_mov_b32_e32 v110, v11
	v_pk_fma_f32 v[106:107], v[114:115], v[114:115], v[106:107]
	v_pk_fma_f32 v[114:115], v[144:145], s[0:1], v[110:111] op_sel_hi:[1,0,1] neg_lo:[1,0,0] neg_hi:[1,0,0]
	v_sub_f32_e32 v118, v112, v135
	v_pk_fma_f32 v[106:107], v[114:115], v[114:115], v[106:107]
	v_mov_b32_e32 v114, v12
	v_mov_b32_e32 v115, v112
	v_pk_fma_f32 v[114:115], v[144:145], s[0:1], v[114:115] op_sel_hi:[1,0,1] neg_lo:[1,0,0] neg_hi:[1,0,0]
	v_mov_b32_e32 v112, v13
	v_pk_fma_f32 v[106:107], v[114:115], v[114:115], v[106:107]
	v_pk_fma_f32 v[114:115], v[144:145], s[0:1], v[112:113] op_sel_hi:[1,0,1] neg_lo:[1,0,0] neg_hi:[1,0,0]
	v_pk_add_f32 v[136:137], v[102:103], v[134:135] op_sel:[0,1] neg_lo:[0,1] neg_hi:[0,1]
	v_pk_fma_f32 v[106:107], v[114:115], v[114:115], v[106:107]
	v_pk_add_f32 v[114:115], v[6:7], v[134:135] op_sel_hi:[1,0] neg_lo:[0,1] neg_hi:[0,1]
	v_pk_mul_f32 v[142:143], v[136:137], v[136:137]
	v_pk_mul_f32 v[114:115], v[114:115], v[114:115]
	v_mov_b32_e32 v117, v142
	v_mov_b32_e32 v116, v114
	v_pk_add_f32 v[136:137], v[104:105], v[134:135] op_sel:[0,1] neg_lo:[0,1] neg_hi:[0,1]
	v_pk_add_f32 v[106:107], v[116:117], v[106:107]
	v_pk_add_f32 v[116:117], v[8:9], v[134:135] op_sel_hi:[1,0] neg_lo:[0,1] neg_hi:[0,1]
	v_pk_mul_f32 v[140:141], v[136:137], v[136:137]
	v_pk_mul_f32 v[116:117], v[116:117], v[116:117]
	v_mov_b32_e32 v142, v115
	v_pk_add_f32 v[136:137], v[98:99], v[134:135] op_sel:[0,1] neg_lo:[0,1] neg_hi:[0,1]
	v_pk_add_f32 v[120:121], v[2:3], v[134:135] op_sel_hi:[1,0] neg_lo:[0,1] neg_hi:[0,1]
	v_pk_add_f32 v[106:107], v[142:143], v[106:107]
	v_mov_b32_e32 v114, v116
	v_mov_b32_e32 v115, v140
	v_pk_mul_f32 v[138:139], v[136:137], v[136:137]
	v_pk_mul_f32 v[120:121], v[120:121], v[120:121]
	v_pk_add_f32 v[106:107], v[114:115], v[106:107]
	v_mov_b32_e32 v140, v117
	v_pk_add_f32 v[136:137], v[100:101], v[134:135] op_sel:[0,1] neg_lo:[0,1] neg_hi:[0,1]
	v_pk_add_f32 v[144:145], v[4:5], v[134:135] op_sel_hi:[1,0] neg_lo:[0,1] neg_hi:[0,1]
	v_pk_add_f32 v[106:107], v[140:141], v[106:107]
	v_mov_b32_e32 v114, v120
	v_mov_b32_e32 v115, v138
	v_pk_mul_f32 v[136:137], v[136:137], v[136:137]
	v_pk_mul_f32 v[144:145], v[144:145], v[144:145]
	v_pk_add_f32 v[106:107], v[114:115], v[106:107]
	v_mov_b32_e32 v138, v121
	v_pk_add_f32 v[106:107], v[138:139], v[106:107]
	v_mov_b32_e32 v114, v144
	v_mov_b32_e32 v115, v136
	v_pk_add_f32 v[106:107], v[114:115], v[106:107]
	v_mov_b32_e32 v136, v145
	v_pk_add_f32 v[106:107], v[136:137], v[106:107]
	ds_bpermute_b32 v115, v149, v107
	ds_bpermute_b32 v114, v149, v106
	v_sub_f32_e32 v121, v109, v135
	v_sub_f32_e32 v116, v102, v135
	v_sub_f32_e32 v112, v98, v135
	v_sub_f32_e32 v120, v111, v135
	s_waitcnt lgkmcnt(0)
	v_pk_add_f32 v[106:107], v[106:107], v[114:115]
	ds_bpermute_b32 v109, v148, v107
	ds_bpermute_b32 v108, v148, v106
	v_sub_f32_e32 v115, v103, v135
	v_sub_f32_e32 v111, v99, v135
	v_sub_f32_e32 v114, v104, v135
	v_lshl_add_u32 v152, v82, 3, v85
	s_waitcnt lgkmcnt(0)
	v_pk_add_f32 v[102:103], v[106:107], v[108:109]
	v_mov_b32_e32 v106, 0x3727c5ac
	v_pk_fma_f32 v[108:109], v[102:103], s[0:1], v[106:107] op_sel_hi:[1,0,0]
	s_mov_b32 s1, 0x800000
	v_mul_f32_e32 v98, 0x4b800000, v109
	v_cmp_gt_f32_e32 vcc, s1, v109
	v_sub_f32_e32 v107, v101, v135
	ds_read_b128 v[82:85], v150 offset:17984
	v_cndmask_b32_e32 v98, v109, v98, vcc
	v_rsq_f32_e32 v98, v98
	v_sub_f32_e32 v109, v100, v135
	ds_read_b128 v[86:89], v150 offset:18496
	v_sub_f32_e32 v117, v113, v135
	v_mul_f32_e32 v99, 0x45800000, v98
	v_cndmask_b32_e32 v110, v98, v99, vcc
	v_mul_f32_e32 v112, v110, v112
	v_fma_f32 v34, v34, v112, v38
	v_mul_f32_e32 v38, v110, v111
	v_fma_f32 v35, v35, v38, v39
	v_max_f32_e32 v38, 0, v35
	v_mul_f32_e32 v35, v110, v109
	v_mul_f32_e32 v116, v110, v116
	v_fma_f32 v35, v36, v35, v40
	v_mul_f32_e32 v36, v110, v107
	v_fma_f32 v42, v42, v116, v46
	v_mul_f32_e32 v46, v110, v115
	v_fmac_f32_e32 v41, v37, v36
	v_mul_f32_e32 v37, 0x4b800000, v108
	v_cmp_gt_f32_e32 vcc, s1, v108
	v_sub_f32_e32 v113, v105, v135
	v_fma_f32 v43, v43, v46, v47
	v_mul_f32_e32 v46, v110, v114
	v_cndmask_b32_e32 v37, v108, v37, vcc
	v_mul_f32_e32 v135, v110, v163
	v_fma_f32 v44, v44, v46, v48
	v_mul_f32_e32 v46, v110, v113
	v_rsq_f32_e32 v37, v37
	v_fma_f32 v90, v90, v135, v94
	v_mul_f32_e32 v94, v110, v162
	v_fmac_f32_e32 v49, v45, v46
	ds_read_b128 v[98:101], v150 offset:17920
	ds_read_b128 v[102:105], v150 offset:18432
	v_fma_f32 v91, v91, v94, v95
	v_mul_f32_e32 v94, v110, v161
	v_max_f32_e32 v42, 0, v42
	v_max_f32_e32 v43, 0, v43
	v_max_f32_e32 v44, 0, v44
	v_max_f32_e32 v45, 0, v49
	v_max_f32_e32 v34, 0, v34
	v_max_f32_e32 v35, 0, v35
	v_max_f32_e32 v36, 0, v41
	v_fma_f32 v92, v92, v94, v96
	v_mul_f32_e32 v94, v110, v160
	v_mul_f32_e32 v135, v110, v159
	v_cvt_pk_f16_f32 v115, v44, v45
	v_cvt_pk_f16_f32 v114, v42, v43
	v_cvt_pk_f16_f32 v35, v35, v36
	v_cvt_pk_f16_f32 v34, v34, v38
	v_fmac_f32_e32 v97, v93, v94
	s_waitcnt lgkmcnt(2)
	v_fma_f32 v82, v82, v135, v86
	v_mul_f32_e32 v86, v110, v158
	ds_write2_b64 v152, v[114:115], v[34:35] offset0:24 offset1:28
	v_mul_f32_e32 v34, 0x45800000, v37
	ds_read_b128 v[66:69], v150 offset:18048
	ds_read_b128 v[70:73], v150 offset:18560
	v_max_f32_e32 v90, 0, v90
	v_max_f32_e32 v91, 0, v91
	v_max_f32_e32 v92, 0, v92
	v_max_f32_e32 v93, 0, v97
	v_fma_f32 v83, v83, v86, v87
	v_cndmask_b32_e32 v34, v37, v34, vcc
	v_sub_f32_e32 v31, v31, v134
	v_cvt_pk_f16_f32 v137, v92, v93
	v_cvt_pk_f16_f32 v136, v90, v91
	ds_read_b128 v[90:93], v150 offset:17984
	ds_read_b128 v[94:97], v150 offset:18496
	v_max_f32_e32 v86, 0, v83
	v_mul_f32_e32 v83, v110, v156
	v_mul_f32_e32 v31, v34, v31
	v_fma_f32 v83, v84, v83, v88
	v_mul_f32_e32 v84, v110, v154
	s_waitcnt lgkmcnt(5)
	v_fma_f32 v31, v99, v31, v103
	ds_read_b128 v[50:53], v150 offset:18112
	ds_read_b128 v[54:57], v150 offset:18624
	v_fmac_f32_e32 v89, v85, v84
	v_max_f32_e32 v35, 0, v31
	v_sub_f32_e32 v31, v32, v134
	v_sub_f32_e32 v32, v33, v134
	v_max_f32_e32 v82, 0, v82
	v_max_f32_e32 v83, 0, v83
	v_max_f32_e32 v84, 0, v89
	v_mul_f32_e32 v135, v110, v153
	v_mul_f32_e32 v31, v34, v31
	v_mul_f32_e32 v32, v34, v32
	v_sub_f32_e32 v27, v27, v134
	v_cvt_pk_f16_f32 v83, v83, v84
	v_cvt_pk_f16_f32 v82, v82, v86
	s_waitcnt lgkmcnt(4)
	v_fma_f32 v66, v66, v135, v70
	v_mul_f32_e32 v70, v110, v157
	v_fma_f32 v31, v100, v31, v104
	v_fmac_f32_e32 v105, v101, v32
	v_mul_f32_e32 v27, v34, v27
	ds_write2_b64 v152, v[136:137], v[82:83] offset1:4
	ds_read_b128 v[82:85], v150 offset:18048
	ds_read_b128 v[86:89], v150 offset:18560
	v_fma_f32 v67, v67, v70, v71
	v_mul_f32_e32 v70, v110, v155
	v_max_f32_e32 v31, 0, v31
	v_max_f32_e32 v32, 0, v105
	s_waitcnt lgkmcnt(5)
	v_fma_f32 v27, v91, v27, v95
	v_fma_f32 v68, v68, v70, v72
	v_mul_f32_e32 v70, v110, v129
	v_mul_f32_e32 v128, v110, v128
	v_sub_f32_e32 v30, v30, v134
	v_cvt_pk_f16_f32 v31, v31, v32
	v_sub_f32_e32 v26, v26, v134
	v_max_f32_e32 v32, 0, v27
	v_sub_f32_e32 v27, v28, v134
	v_sub_f32_e32 v28, v29, v134
	v_fmac_f32_e32 v73, v69, v70
	s_waitcnt lgkmcnt(3)
	v_fma_f32 v50, v50, v128, v54
	v_mul_f32_e32 v54, v110, v127
	v_mul_f32_e32 v30, v34, v30
	v_mul_f32_e32 v26, v34, v26
	v_mul_f32_e32 v27, v34, v27
	v_mul_f32_e32 v28, v34, v28
	ds_read_b128 v[74:77], v150 offset:18176
	ds_read_b128 v[78:81], v150 offset:18688
	v_max_f32_e32 v66, 0, v66
	v_max_f32_e32 v67, 0, v67
	v_max_f32_e32 v68, 0, v68
	v_max_f32_e32 v69, 0, v73
	v_fma_f32 v51, v51, v54, v55
	v_fma_f32 v30, v98, v30, v102
	v_fma_f32 v26, v90, v26, v94
	v_fma_f32 v27, v92, v27, v96
	v_fmac_f32_e32 v97, v93, v28
	v_sub_f32_e32 v23, v23, v134
	v_cvt_pk_f16_f32 v137, v68, v69
	v_cvt_pk_f16_f32 v136, v66, v67
	ds_read_b128 v[66:69], v150 offset:18112
	ds_read_b128 v[70:73], v150 offset:18624
	v_max_f32_e32 v54, 0, v51
	v_mul_f32_e32 v51, v110, v126
	v_max_f32_e32 v30, 0, v30
	v_max_f32_e32 v26, 0, v26
	v_max_f32_e32 v27, 0, v27
	v_max_f32_e32 v28, 0, v97
	v_mul_f32_e32 v23, v34, v23
	v_fma_f32 v51, v52, v51, v56
	v_mul_f32_e32 v52, v110, v125
	v_cvt_pk_f16_f32 v30, v30, v35
	v_cvt_pk_f16_f32 v27, v27, v28
	v_cvt_pk_f16_f32 v26, v26, v32
	v_add_u32_e32 v28, 0x1000, v152
	s_waitcnt lgkmcnt(4)
	v_fma_f32 v23, v83, v23, v87
	ds_read_b128 v[58:61], v150 offset:18240
	ds_read_b128 v[62:65], v150 offset:18752
	v_fmac_f32_e32 v57, v53, v52
	ds_write2_b64 v28, v[30:31], v[26:27] offset0:32 offset1:36
	v_max_f32_e32 v26, 0, v23
	v_sub_f32_e32 v23, v24, v134
	v_sub_f32_e32 v24, v25, v134
	v_max_f32_e32 v50, 0, v50
	v_max_f32_e32 v51, 0, v51
	v_max_f32_e32 v52, 0, v57
	v_mul_f32_e32 v124, v110, v124
	v_mul_f32_e32 v23, v34, v23
	v_mul_f32_e32 v24, v34, v24
	v_sub_f32_e32 v19, v19, v134
	v_cvt_pk_f16_f32 v51, v51, v52
	v_cvt_pk_f16_f32 v50, v50, v54
	s_waitcnt lgkmcnt(5)
	v_fma_f32 v74, v74, v124, v78
	v_mul_f32_e32 v78, v110, v123
	v_fma_f32 v23, v84, v23, v88
	v_fmac_f32_e32 v89, v85, v24
	v_mul_f32_e32 v19, v34, v19
	ds_write2_b64 v152, v[136:137], v[50:51] offset0:8 offset1:12
	ds_read_b128 v[50:53], v150 offset:18176
	ds_read_b128 v[54:57], v150 offset:18688
	v_fma_f32 v75, v75, v78, v79
	v_mul_f32_e32 v78, v110, v122
	v_max_f32_e32 v23, 0, v23
	v_max_f32_e32 v24, 0, v89
	s_waitcnt lgkmcnt(6)
	v_fma_f32 v19, v67, v19, v71
	v_fma_f32 v76, v76, v78, v80
	v_mul_f32_e32 v78, v110, v121
	v_mul_f32_e32 v119, v110, v119
	v_sub_f32_e32 v22, v22, v134
	v_cvt_pk_f16_f32 v23, v23, v24
	v_sub_f32_e32 v18, v18, v134
	v_max_f32_e32 v24, 0, v19
	v_sub_f32_e32 v19, v20, v134
	v_sub_f32_e32 v20, v21, v134
	v_fmac_f32_e32 v81, v77, v78
	s_waitcnt lgkmcnt(4)
	v_fma_f32 v58, v58, v119, v62
	v_mul_f32_e32 v62, v110, v120
	v_mul_f32_e32 v22, v34, v22
	v_mul_f32_e32 v18, v34, v18
	v_mul_f32_e32 v19, v34, v19
	v_mul_f32_e32 v20, v34, v20
	v_max_f32_e32 v74, 0, v74
	v_max_f32_e32 v75, 0, v75
	v_max_f32_e32 v76, 0, v76
	v_max_f32_e32 v77, 0, v81
	v_fma_f32 v59, v59, v62, v63
	v_fma_f32 v22, v82, v22, v86
	v_fma_f32 v18, v66, v18, v70
	v_fma_f32 v19, v68, v19, v72
	v_fmac_f32_e32 v73, v69, v20
	v_sub_f32_e32 v15, v15, v134
	v_cvt_pk_f16_f32 v123, v76, v77
	v_cvt_pk_f16_f32 v122, v74, v75
	ds_read_b128 v[74:77], v150 offset:18240
	ds_read_b128 v[78:81], v150 offset:18752
	v_max_f32_e32 v62, 0, v59
	v_mul_f32_e32 v59, v110, v118
	v_max_f32_e32 v22, 0, v22
	v_max_f32_e32 v18, 0, v18
	v_max_f32_e32 v19, 0, v19
	v_max_f32_e32 v20, 0, v73
	v_mul_f32_e32 v15, v34, v15
	v_fma_f32 v59, v60, v59, v64
	v_mul_f32_e32 v60, v110, v117
	v_cvt_pk_f16_f32 v22, v22, v26
	v_cvt_pk_f16_f32 v19, v19, v20
	v_cvt_pk_f16_f32 v18, v18, v24
	s_waitcnt lgkmcnt(2)
	v_fma_f32 v15, v51, v15, v55
	v_fmac_f32_e32 v65, v61, v60
	ds_write2_b64 v28, v[22:23], v[18:19] offset0:40 offset1:44
	v_max_f32_e32 v18, 0, v15
	v_sub_f32_e32 v15, v16, v134
	v_sub_f32_e32 v16, v17, v134
	v_max_f32_e32 v58, 0, v58
	v_max_f32_e32 v59, 0, v59
	v_max_f32_e32 v60, 0, v65
	v_mul_f32_e32 v15, v34, v15
	v_mul_f32_e32 v16, v34, v16
	v_sub_f32_e32 v11, v11, v134
	v_cvt_pk_f16_f32 v59, v59, v60
	v_cvt_pk_f16_f32 v58, v58, v62
	v_fma_f32 v15, v52, v15, v56
	v_fmac_f32_e32 v57, v53, v16
	v_mul_f32_e32 v11, v34, v11
	ds_write2_b64 v152, v[122:123], v[58:59] offset0:16 offset1:20
	ds_read_b128 v[58:61], v150 offset:18304
	ds_read_b128 v[62:65], v150 offset:18816
	v_max_f32_e32 v15, 0, v15
	v_max_f32_e32 v16, 0, v57
	s_waitcnt lgkmcnt(4)
	v_fma_f32 v11, v75, v11, v79
	v_sub_f32_e32 v14, v14, v134
	v_cvt_pk_f16_f32 v15, v15, v16
	v_sub_f32_e32 v10, v10, v134
	v_max_f32_e32 v16, 0, v11
	v_sub_f32_e32 v11, v12, v134
	v_sub_f32_e32 v12, v13, v134
	v_mul_f32_e32 v14, v34, v14
	v_mul_f32_e32 v10, v34, v10
	v_mul_f32_e32 v11, v34, v11
	v_mul_f32_e32 v12, v34, v12
	v_fma_f32 v14, v50, v14, v54
	v_fma_f32 v10, v74, v10, v78
	v_fma_f32 v11, v76, v11, v80
	v_fmac_f32_e32 v81, v77, v12
	v_sub_f32_e32 v7, v7, v134
	ds_read_b128 v[42:45], v150 offset:18368
	ds_read_b128 v[46:49], v150 offset:18880
	v_max_f32_e32 v14, 0, v14
	v_max_f32_e32 v10, 0, v10
	v_max_f32_e32 v11, 0, v11
	v_max_f32_e32 v12, 0, v81
	v_mul_f32_e32 v7, v34, v7
	v_cvt_pk_f16_f32 v14, v14, v18
	v_cvt_pk_f16_f32 v11, v11, v12
	v_cvt_pk_f16_f32 v10, v10, v16
	s_waitcnt lgkmcnt(2)
	v_fma_f32 v7, v59, v7, v63
	ds_write2_b64 v28, v[14:15], v[10:11] offset0:48 offset1:52
	v_max_f32_e32 v10, 0, v7
	v_sub_f32_e32 v7, v8, v134
	v_sub_f32_e32 v8, v9, v134
	v_mul_f32_e32 v7, v34, v7
	v_mul_f32_e32 v8, v34, v8
	v_sub_f32_e32 v3, v3, v134
	v_fma_f32 v7, v60, v7, v64
	v_fmac_f32_e32 v65, v61, v8
	v_mul_f32_e32 v3, v34, v3
	v_max_f32_e32 v7, 0, v7
	v_max_f32_e32 v8, 0, v65
	s_waitcnt lgkmcnt(1)
	v_fma_f32 v3, v43, v3, v47
	v_sub_f32_e32 v6, v6, v134
	v_cvt_pk_f16_f32 v7, v7, v8
	v_sub_f32_e32 v2, v2, v134
	v_max_f32_e32 v8, 0, v3
	v_sub_f32_e32 v3, v4, v134
	v_sub_f32_e32 v4, v5, v134
	v_mul_f32_e32 v6, v34, v6
	v_mul_f32_e32 v2, v34, v2
	v_mul_f32_e32 v3, v34, v3
	v_mul_f32_e32 v4, v34, v4
	v_fma_f32 v6, v58, v6, v62
	v_fma_f32 v2, v42, v2, v46
	v_fma_f32 v3, v44, v3, v48
	v_fmac_f32_e32 v49, v45, v4
	v_max_f32_e32 v6, 0, v6
	v_max_f32_e32 v2, 0, v2
	v_max_f32_e32 v3, 0, v3
	v_max_f32_e32 v4, 0, v49
	v_cvt_pk_f16_f32 v6, v6, v10
	v_cvt_pk_f16_f32 v3, v3, v4
	v_cvt_pk_f16_f32 v2, v2, v8
	ds_write2_b64 v28, v[6:7], v[2:3] offset0:56 offset1:60
	v_lshl_add_u64 v[34:35], s[36:37], 0, v[132:133]
	v_add_co_u32_e32 v74, vcc, s9, v34
	global_load_dwordx4 v[66:69], v132, s[36:37]
	s_nop 0
	v_addc_co_u32_e32 v75, vcc, 0, v35, vcc
	v_add_co_u32_e32 v76, vcc, s11, v34
	ds_read_b128 v[116:119], v151
	s_nop 0
	v_addc_co_u32_e32 v77, vcc, 0, v35, vcc
	global_load_dwordx4 v[88:91], v[76:77], off offset:-4096
	v_add_co_u32_e32 v78, vcc, s12, v34
	global_load_dwordx4 v[70:73], v[76:77], off
	s_nop 0
	v_addc_co_u32_e32 v79, vcc, 0, v35, vcc
	v_add_co_u32_e32 v80, vcc, s8, v34
	ds_read_b128 v[120:123], v151 offset:4352
	s_nop 0
	v_addc_co_u32_e32 v81, vcc, 0, v35, vcc
	global_load_dwordx4 v[92:95], v[80:81], off offset:-4096
	v_add_co_u32_e32 v82, vcc, s10, v34
	global_load_dwordx4 v[96:99], v[80:81], off
	s_nop 0
	v_addc_co_u32_e32 v83, vcc, 0, v35, vcc
	v_add_co_u32_e32 v84, vcc, s7, v34
	ds_read_b128 v[164:167], v151 offset:4416
	s_nop 0
	v_addc_co_u32_e32 v85, vcc, 0, v35, vcc
	global_load_dwordx4 v[108:111], v[84:85], off
	global_load_dwordx4 v[100:103], v[84:85], off offset:-4096
	v_add_co_u32_e32 v86, vcc, s6, v34
	s_nop 1
	v_addc_co_u32_e32 v87, vcc, 0, v35, vcc
	global_load_dwordx4 v[112:115], v[86:87], off
	global_load_dwordx4 v[58:61], v132, s[36:37] offset:1024
	global_load_dwordx4 v[62:65], v[74:75], off offset:1024
	global_load_dwordx4 v[34:37], v[76:77], off offset:1024
	global_load_dwordx4 v[54:57], v[78:79], off offset:1024
	global_load_dwordx4 v[50:53], v[80:81], off offset:1024
	global_load_dwordx4 v[46:49], v[82:83], off offset:1024
	global_load_dwordx4 v[42:45], v[84:85], off offset:1024
	global_load_dwordx4 v[38:41], v[86:87], off offset:1024
	ds_read_b128 v[30:33], v147 offset:18944
	ds_read_b128 v[26:29], v147 offset:19008
	s_waitcnt vmcnt(15) lgkmcnt(1)
	v_mfma_f32_16x16x32_f16 v[124:127], v[66:69], v[116:119], v[30:33]
	v_mfma_f32_16x16x32_f16 v[66:69], v[66:69], v[120:123], v[30:33]
	s_waitcnt vmcnt(14) lgkmcnt(0)
	v_mfma_f32_16x16x32_f16 v[134:137], v[88:91], v[116:119], v[26:29]
	v_mfma_f32_16x16x32_f16 v[88:91], v[88:91], v[120:123], v[26:29]
	global_load_dwordx4 v[30:33], v132, s[36:37] offset:2048
	s_nop 1
	global_load_dwordx4 v[26:29], v[74:75], off offset:2048
	ds_read_b128 v[22:25], v147 offset:19072
	ds_read_b128 v[18:21], v147 offset:19136
	s_waitcnt vmcnt(15) lgkmcnt(1)
	v_mfma_f32_16x16x32_f16 v[138:141], v[70:73], v[116:119], v[22:25]
	v_mfma_f32_16x16x32_f16 v[70:73], v[70:73], v[120:123], v[22:25]
	s_waitcnt vmcnt(14) lgkmcnt(0)
	v_mfma_f32_16x16x32_f16 v[142:145], v[92:95], v[116:119], v[18:21]
	v_mfma_f32_16x16x32_f16 v[92:95], v[92:95], v[120:123], v[18:21]
	global_load_dwordx4 v[22:25], v[76:77], off offset:2048
	s_nop 1
	global_load_dwordx4 v[18:21], v[78:79], off offset:2048
	ds_read_b128 v[6:9], v147 offset:19328
	s_waitcnt vmcnt(14) lgkmcnt(0)
	v_mfma_f32_16x16x32_f16 v[160:163], v[108:111], v[116:119], v[6:9]
	v_mfma_f32_16x16x32_f16 v[108:111], v[108:111], v[120:123], v[6:9]
	s_nop 2
	global_load_dwordx4 v[6:9], v[84:85], off offset:2048
	ds_read_b128 v[10:13], v147 offset:19264
	s_waitcnt vmcnt(14) lgkmcnt(0)
	v_mfma_f32_16x16x32_f16 v[156:159], v[100:103], v[116:119], v[10:13]
	v_mfma_f32_16x16x32_f16 v[100:103], v[100:103], v[120:123], v[10:13]
	s_nop 2
	global_load_dwordx4 v[10:13], v[82:83], off offset:2048
	ds_read_b128 v[14:17], v147 offset:19200
	s_waitcnt lgkmcnt(0)
	v_mfma_f32_16x16x32_f16 v[152:155], v[96:99], v[116:119], v[14:17]
	ds_read_b128 v[2:5], v147 offset:19392
	s_waitcnt vmcnt(14) lgkmcnt(0)
	v_mfma_f32_16x16x32_f16 v[116:119], v[112:115], v[116:119], v[2:5]
	v_mfma_f32_16x16x32_f16 v[112:115], v[112:115], v[120:123], v[2:5]
	s_nop 2
	global_load_dwordx4 v[2:5], v[86:87], off offset:2048
	v_mfma_f32_16x16x32_f16 v[96:99], v[96:99], v[120:123], v[14:17]
	ds_read_b128 v[120:123], v151 offset:64
	s_nop 1
	global_load_dwordx4 v[14:17], v[80:81], off offset:2048
	s_waitcnt vmcnt(15) lgkmcnt(0)
	v_mfma_f32_16x16x32_f16 v[124:127], v[58:61], v[120:123], v[124:127]
	v_mfma_f32_16x16x32_f16 v[58:61], v[58:61], v[164:167], v[66:69]
	s_waitcnt vmcnt(14)
	v_mfma_f32_16x16x32_f16 v[66:69], v[62:65], v[120:123], v[134:137]
	v_mfma_f32_16x16x32_f16 v[62:65], v[62:65], v[164:167], v[88:91]
	s_nop 1
	global_load_dwordx4 v[134:137], v[82:83], off offset:3072
	s_nop 0
	global_load_dwordx4 v[82:85], v[84:85], off offset:3072
	s_waitcnt vmcnt(15)
	v_mfma_f32_16x16x32_f16 v[88:91], v[34:37], v[120:123], v[138:141]
	v_mfma_f32_16x16x32_f16 v[34:37], v[34:37], v[164:167], v[70:73]
	s_nop 1
	global_load_dwordx4 v[138:141], v[86:87], off offset:3072
	s_waitcnt vmcnt(15)
	v_mfma_f32_16x16x32_f16 v[70:73], v[54:57], v[120:123], v[142:145]
	v_mfma_f32_16x16x32_f16 v[54:57], v[54:57], v[164:167], v[92:95]
	s_nop 1
	ds_read_b128 v[142:145], v151 offset:128
	s_waitcnt vmcnt(14)
	v_mfma_f32_16x16x32_f16 v[92:95], v[50:53], v[120:123], v[152:155]
	v_mfma_f32_16x16x32_f16 v[50:53], v[50:53], v[164:167], v[96:99]
	s_nop 1
	ds_read_b128 v[152:155], v151 offset:4480
	s_waitcnt vmcnt(13)
	v_mfma_f32_16x16x32_f16 v[96:99], v[46:49], v[120:123], v[156:159]
	v_mfma_f32_16x16x32_f16 v[46:49], v[46:49], v[164:167], v[100:103]
	s_waitcnt vmcnt(12)
	v_mfma_f32_16x16x32_f16 v[100:103], v[42:45], v[120:123], v[160:163]
	v_mfma_f32_16x16x32_f16 v[42:45], v[42:45], v[164:167], v[108:111]
	s_waitcnt vmcnt(11)
	v_mfma_f32_16x16x32_f16 v[108:111], v[38:41], v[120:123], v[116:119]
	global_load_dwordx4 v[120:123], v[78:79], off offset:3072
	s_nop 0
	global_load_dwordx4 v[78:81], v[80:81], off offset:3072
	s_nop 0
	global_load_dwordx4 v[116:119], v[74:75], off offset:3072
	v_mfma_f32_16x16x32_f16 v[38:41], v[38:41], v[164:167], v[112:115]
	global_load_dwordx4 v[74:77], v[76:77], off offset:3072
	s_nop 1
	global_load_dwordx4 v[112:115], v132, s[36:37] offset:3072
	s_waitcnt vmcnt(15) lgkmcnt(1)
	v_mfma_f32_16x16x32_f16 v[124:127], v[30:33], v[142:145], v[124:127]
	s_waitcnt lgkmcnt(0)
	v_mfma_f32_16x16x32_f16 v[30:33], v[30:33], v[152:155], v[58:61]
	s_waitcnt vmcnt(14)
	v_mfma_f32_16x16x32_f16 v[58:61], v[26:29], v[142:145], v[66:69]
	v_mfma_f32_16x16x32_f16 v[26:29], v[26:29], v[152:155], v[62:65]
	s_waitcnt vmcnt(13)
	v_mfma_f32_16x16x32_f16 v[62:65], v[22:25], v[142:145], v[88:91]
	v_mfma_f32_16x16x32_f16 v[22:25], v[22:25], v[152:155], v[34:37]
	s_waitcnt vmcnt(12)
	v_mfma_f32_16x16x32_f16 v[34:37], v[18:21], v[142:145], v[70:73]
	s_waitcnt vmcnt(8)
	v_mfma_f32_16x16x32_f16 v[66:69], v[14:17], v[142:145], v[92:95]
	v_mfma_f32_16x16x32_f16 v[86:89], v[10:13], v[142:145], v[96:99]
	v_mfma_f32_16x16x32_f16 v[94:97], v[6:9], v[142:145], v[100:103]
	v_mfma_f32_16x16x32_f16 v[102:105], v[2:5], v[142:145], v[108:111]
	ds_read_b128 v[142:145], v151 offset:4544
	s_nop 1
	ds_read_b128 v[108:111], v151 offset:192
	v_mfma_f32_16x16x32_f16 v[18:21], v[18:21], v[152:155], v[54:57]
	v_mfma_f32_16x16x32_f16 v[70:73], v[14:17], v[152:155], v[50:53]
	v_mfma_f32_16x16x32_f16 v[90:93], v[10:13], v[152:155], v[46:49]
	v_mfma_f32_16x16x32_f16 v[98:101], v[6:9], v[152:155], v[42:45]
	v_mfma_f32_16x16x32_f16 v[2:5], v[2:5], v[152:155], v[38:41]
	s_waitcnt vmcnt(0) lgkmcnt(1)
	v_mfma_f32_16x16x32_f16 v[6:9], v[112:115], v[142:145], v[30:33]
	s_waitcnt lgkmcnt(0)
	v_mfma_f32_16x16x32_f16 v[50:53], v[116:119], v[108:111], v[58:61]
	v_mfma_f32_16x16x32_f16 v[10:13], v[116:119], v[142:145], v[26:29]
	v_mfma_f32_16x16x32_f16 v[54:57], v[74:77], v[108:111], v[62:65]
	v_mfma_f32_16x16x32_f16 v[14:17], v[74:77], v[142:145], v[22:25]
	v_mfma_f32_16x16x32_f16 v[18:21], v[120:123], v[142:145], v[18:21]
	v_mfma_f32_16x16x32_f16 v[22:25], v[78:81], v[142:145], v[70:73]
	v_mfma_f32_16x16x32_f16 v[26:29], v[134:137], v[142:145], v[90:93]
	v_mfma_f32_16x16x32_f16 v[30:33], v[82:85], v[142:145], v[98:101]
	v_mfma_f32_16x16x32_f16 v[2:5], v[138:141], v[142:145], v[2:5]
	v_mfma_f32_16x16x32_f16 v[46:49], v[112:115], v[108:111], v[124:127]
	v_mfma_f32_16x16x32_f16 v[58:61], v[120:123], v[108:111], v[34:37]
	v_mfma_f32_16x16x32_f16 v[62:65], v[78:81], v[108:111], v[66:69]
	v_mfma_f32_16x16x32_f16 v[42:45], v[134:137], v[108:111], v[86:89]
	v_mfma_f32_16x16x32_f16 v[38:41], v[82:85], v[108:111], v[94:97]
	v_mfma_f32_16x16x32_f16 v[34:37], v[138:141], v[108:111], v[102:105]
	s_nop 2
	v_lshrrev_b32_e32 v104, 5, v146
	v_lshlrev_b32_e32 v66, 2, v104
	v_lshl_or_b32 v105, v1, 7, v66
	ds_read_b32 v70, v105 offset:20480
	ds_read_b128 v[112:115], v150 offset:19776
	v_add_u32_e32 v82, 0x5000, v105
	ds_read2_b32 v[68:69], v82 offset1:2
	ds_read2_b32 v[78:79], v82 offset0:4 offset1:6
	v_lshlrev_b32_e32 v0, 4, v0
	v_and_b32_e32 v132, 0x1f0, v0
	v_lshl_add_u64 v[66:67], s[4:5], 0, v[132:133]
	v_add_u32_e32 v83, v130, v132
	v_lshl_add_u64 v[0:1], s[2:3], 0, v[132:133]
	ds_read2_b32 v[80:81], v82 offset0:8 offset1:10
	s_waitcnt lgkmcnt(4)
	v_max_i32_e32 v132, 0, v70
	v_lshlrev_b64 v[70:71], 9, v[132:133]
	s_waitcnt lgkmcnt(2)
	v_max_i32_e32 v132, 0, v69
	v_lshlrev_b64 v[72:73], 9, v[132:133]
	s_waitcnt lgkmcnt(1)
	v_max_i32_e32 v132, 0, v78
	v_lshlrev_b64 v[84:85], 9, v[132:133]
	v_max_i32_e32 v132, 0, v79
	v_lshlrev_b64 v[78:79], 9, v[132:133]
	v_lshl_add_u64 v[84:85], v[66:67], 0, v[84:85]
	v_lshl_add_u64 v[78:79], v[66:67], 0, v[78:79]
	s_waitcnt lgkmcnt(0)
	v_max_i32_e32 v132, 0, v80
	global_load_dwordx4 v[84:87], v[84:85], off nt
	v_lshl_add_u64 v[70:71], v[66:67], 0, v[70:71]
	global_load_dwordx4 v[88:91], v[78:79], off nt
	v_lshlrev_b64 v[78:79], 9, v[132:133]
	v_max_i32_e32 v132, 0, v81
	ds_read2_b32 v[80:81], v82 offset0:12 offset1:14
	v_lshlrev_b64 v[92:93], 9, v[132:133]
	v_lshl_add_u64 v[78:79], v[66:67], 0, v[78:79]
	v_lshl_add_u64 v[96:97], v[66:67], 0, v[92:93]
	global_load_dwordx4 v[92:95], v[78:79], off nt
	s_waitcnt lgkmcnt(0)
	v_max_i32_e32 v132, 0, v80
	global_load_dwordx4 v[96:99], v[96:97], off nt
	v_lshlrev_b64 v[78:79], 9, v[132:133]
	v_max_i32_e32 v132, 0, v81
	v_lshlrev_b64 v[80:81], 9, v[132:133]
	v_lshl_add_u64 v[74:75], v[66:67], 0, v[72:73]
	v_lshl_add_u64 v[78:79], v[66:67], 0, v[78:79]
	v_lshl_add_u64 v[80:81], v[66:67], 0, v[80:81]
	global_load_dwordx4 v[70:73], v[70:71], off nt
	s_movk_i32 s2, 0x220
	global_load_dwordx4 v[74:77], v[74:75], off nt
	v_mov_b32_e32 v69, 0x440
	global_load_dwordx4 v[100:103], v[78:79], off nt
	global_load_dwordx4 v[108:111], v[80:81], off nt
	v_mov_b32_e32 v78, 0x880
	v_mad_u32_u24 v69, v104, s2, v69
	v_mad_u32_u24 v78, v104, s2, v78
	v_mad_u32_u24 v107, v131, s2, v130
	v_mad_u32_u24 v79, v104, s2, v83
	v_add_u32_e32 v81, v83, v69
	v_add_u32_e32 v80, v83, v78
	v_add_u32_e32 v82, v107, v147
	s_load_dword s0, s[34:35], 0x0
	v_mul_u32_u24_e32 v69, 0x220, v104
	ds_read_b128 v[120:123], v150 offset:20288
	ds_read_b128 v[128:131], v150 offset:20352
	ds_read_b128 v[134:137], v150 offset:20416
	ds_read_b128 v[116:119], v150 offset:20224
	ds_read_b128 v[124:127], v150 offset:19904
	s_waitcnt vmcnt(7)
	ds_write_b128 v80, v[84:87]
	s_waitcnt vmcnt(6)
	ds_write_b128 v80, v[88:91] offset:1088
	s_waitcnt vmcnt(5)
	ds_write_b128 v80, v[92:95] offset:2176
	s_waitcnt vmcnt(4)
	ds_write_b128 v80, v[96:99] offset:3264
	s_waitcnt vmcnt(3)
	ds_write_b128 v79, v[70:73]
	s_waitcnt vmcnt(2)
	ds_write_b128 v81, v[74:77]
	s_waitcnt vmcnt(1)
	ds_write_b128 v80, v[100:103] offset:4352
	s_waitcnt vmcnt(0)
	ds_write_b128 v80, v[108:111] offset:5440
	ds_read_b128 v[70:73], v82
	ds_read_b128 v[84:87], v82 offset:64
	ds_read_b128 v[88:91], v82 offset:128
	ds_read_b128 v[92:95], v82 offset:192
	ds_read_b128 v[96:99], v82 offset:256
	ds_read_b128 v[100:103], v82 offset:320
	s_waitcnt lgkmcnt(0)
	v_pk_fma_f32 v[78:79], s[0:1], v[46:47], v[70:71] op_sel_hi:[0,1,1]
	v_pk_fma_f32 v[76:77], s[0:1], v[48:49], v[72:73] op_sel_hi:[0,1,1]
	v_pk_fma_f32 v[74:75], s[0:1], v[50:51], v[84:85] op_sel_hi:[0,1,1]
	v_pk_fma_f32 v[72:73], s[0:1], v[52:53], v[86:87] op_sel_hi:[0,1,1]
	v_pk_fma_f32 v[70:71], s[0:1], v[54:55], v[88:89] op_sel_hi:[0,1,1]
	v_pk_fma_f32 v[54:55], s[0:1], v[56:57], v[90:91] op_sel_hi:[0,1,1]
	v_pk_fma_f32 v[52:53], s[0:1], v[58:59], v[92:93] op_sel_hi:[0,1,1]
	v_pk_fma_f32 v[50:51], s[0:1], v[60:61], v[94:95] op_sel_hi:[0,1,1]
	v_pk_fma_f32 v[48:49], s[0:1], v[62:63], v[96:97] op_sel_hi:[0,1,1]
	v_mov_b32_e32 v56, v78
	v_mov_b32_e32 v57, v74
	v_mov_b32_e32 v58, v79
	v_mov_b32_e32 v59, v75
	v_mov_b32_e32 v60, v76
	v_mov_b32_e32 v61, v72
	v_mov_b32_e32 v62, v77
	v_mov_b32_e32 v63, v73
	v_pk_fma_f32 v[46:47], s[0:1], v[64:65], v[98:99] op_sel_hi:[0,1,1]
	v_mov_b32_e32 v64, v70
	v_mov_b32_e32 v65, v54
	v_mov_b32_e32 v84, v71
	v_mov_b32_e32 v85, v55
	v_pk_add_f32 v[56:57], v[56:57], v[58:59]
	v_pk_add_f32 v[58:59], v[60:61], v[62:63]
	v_pk_add_f32 v[60:61], v[64:65], v[84:85]
	v_pk_add_f32 v[56:57], v[56:57], v[58:59]
	v_pk_add_f32 v[86:87], v[52:53], v[52:53] op_sel:[0,1] op_sel_hi:[1,0]
	v_pk_add_f32 v[88:89], v[50:51], v[50:51] op_sel:[0,1] op_sel_hi:[1,0]
	v_pk_add_f32 v[58:59], v[60:61], v[60:61] op_sel:[0,1] op_sel_hi:[1,0]
	v_add_f32_e32 v56, 0, v56
	v_mov_b32_e32 v91, v48
	v_mov_b32_e32 v87, v46
	v_mov_b32_e32 v89, v47
	v_mov_b32_e32 v59, v49
	v_add_f32_e32 v90, v56, v57
	v_pk_fma_f32 v[42:43], s[0:1], v[42:43], v[100:101] op_sel_hi:[0,1,1]
	v_pk_fma_f32 v[44:45], s[0:1], v[44:45], v[102:103] op_sel_hi:[0,1,1]
	v_pk_add_f32 v[60:61], v[86:87], v[88:89]
	v_pk_add_f32 v[56:57], v[90:91], v[58:59]
	v_mov_b32_e32 v92, v42
	v_pk_add_f32 v[56:57], v[56:57], v[60:61]
	v_mov_b32_e32 v93, v44
	v_mov_b32_e32 v60, v43
	v_mov_b32_e32 v61, v45
	v_pk_add_f32 v[64:65], v[56:57], v[56:57] op_sel:[0,1] op_sel_hi:[1,0]
	ds_read_b128 v[56:59], v82 offset:384
	v_pk_add_f32 v[60:61], v[92:93], v[60:61]
	ds_read_b128 v[96:99], v150 offset:20096
	v_pk_add_f32 v[84:85], v[60:61], v[60:61] op_sel:[0,1] op_sel_hi:[1,0]
	ds_read_b128 v[60:63], v82 offset:448
	s_waitcnt lgkmcnt(2)
	v_pk_fma_f32 v[88:89], s[0:1], v[38:39], v[56:57] op_sel_hi:[0,1,1]
	v_pk_fma_f32 v[40:41], s[0:1], v[40:41], v[58:59] op_sel_hi:[0,1,1]
	v_pk_add_f32 v[38:39], v[88:89], v[88:89] op_sel:[0,1] op_sel_hi:[1,0]
	v_pk_add_f32 v[56:57], v[40:41], v[40:41] op_sel:[0,1] op_sel_hi:[1,0]
	s_waitcnt lgkmcnt(0)
	v_pk_fma_f32 v[90:91], s[0:1], v[34:35], v[60:61] op_sel_hi:[0,1,1]
	v_pk_fma_f32 v[92:93], s[0:1], v[36:37], v[62:63] op_sel_hi:[0,1,1]
	v_mov_b32_e32 v65, v90
	v_mov_b32_e32 v85, v91
	v_mov_b32_e32 v39, v92
	v_mov_b32_e32 v57, v93
	v_pk_add_f32 v[34:35], v[64:65], v[84:85]
	v_pk_add_f32 v[36:37], v[38:39], v[56:57]
	ds_read_b128 v[62:65], v150 offset:19968
	v_pk_add_f32 v[34:35], v[34:35], v[36:37]
	ds_read_b128 v[36:39], v150 offset:19456
	ds_read_b128 v[58:61], v150 offset:19520
	v_add_f32_e32 v34, v34, v35
	ds_bpermute_b32 v35, v149, v34
	ds_read_b128 v[84:87], v150 offset:20032
	v_add_u32_e32 v57, v107, v150
	ds_read_b128 v[100:103], v150 offset:20160
	ds_read_b128 v[108:111], v150 offset:19712
	s_waitcnt lgkmcnt(3)
	v_add_f32_e32 v34, v34, v35
	ds_bpermute_b32 v35, v148, v34
	v_or_b32_e32 v56, 0x5000, v105
	s_waitcnt lgkmcnt(0)
	v_add_f32_e32 v35, v34, v35
	v_fmamk_f32 v95, v35, 0xbc000000, v79
	v_fmamk_f32 v94, v35, 0xbc000000, v78
	v_mul_f32_e32 v95, v95, v95
	v_fmac_f32_e32 v95, v94, v94
	v_fmamk_f32 v94, v35, 0xbc000000, v76
	v_fmac_f32_e32 v95, v94, v94
	v_fmamk_f32 v94, v35, 0xbc000000, v77
	v_fmac_f32_e32 v95, v94, v94
	v_fmamk_f32 v94, v35, 0xbc000000, v74
	v_fmac_f32_e32 v95, v94, v94
	v_fmamk_f32 v94, v35, 0xbc000000, v75
	v_fmac_f32_e32 v95, v94, v94
	v_fmamk_f32 v94, v35, 0xbc000000, v72
	v_fmac_f32_e32 v95, v94, v94
	v_fmamk_f32 v94, v35, 0xbc000000, v73
	v_fmac_f32_e32 v95, v94, v94
	v_fmamk_f32 v94, v35, 0xbc000000, v70
	v_fmac_f32_e32 v95, v94, v94
	v_fmamk_f32 v94, v35, 0xbc000000, v71
	v_fmac_f32_e32 v95, v94, v94
	v_fmamk_f32 v94, v35, 0xbc000000, v54
	v_fmac_f32_e32 v95, v94, v94
	v_fmamk_f32 v94, v35, 0xbc000000, v55
	v_fmac_f32_e32 v95, v94, v94
	v_fmamk_f32 v94, v35, 0xbc000000, v52
	v_fmac_f32_e32 v95, v94, v94
	v_fmamk_f32 v94, v35, 0xbc000000, v53
	v_fmac_f32_e32 v95, v94, v94
	v_fmamk_f32 v94, v35, 0xbc000000, v50
	v_fmac_f32_e32 v95, v94, v94
	v_fmamk_f32 v94, v35, 0xbc000000, v51
	v_fmac_f32_e32 v95, v94, v94
	v_fmamk_f32 v94, v35, 0xbc000000, v48
	v_fmac_f32_e32 v95, v94, v94
	v_fmamk_f32 v94, v35, 0xbc000000, v49
	v_fmac_f32_e32 v95, v94, v94
	v_fmamk_f32 v94, v35, 0xbc000000, v46
	v_fmac_f32_e32 v95, v94, v94
	v_fmamk_f32 v94, v35, 0xbc000000, v47
	v_fmac_f32_e32 v95, v94, v94
	v_fmamk_f32 v94, v35, 0xbc000000, v42
	v_fmac_f32_e32 v95, v94, v94
	v_fmamk_f32 v94, v35, 0xbc000000, v43
	v_mul_f32_e32 v34, 0x3c000000, v35
	v_fmac_f32_e32 v95, v94, v94
	v_fmamk_f32 v94, v35, 0xbc000000, v44
	v_fmamk_f32 v35, v35, 0xbc000000, v45
	v_fmac_f32_e32 v95, v94, v94
	v_pk_add_f32 v[138:139], v[88:89], v[34:35] op_sel_hi:[1,0] neg_lo:[0,1] neg_hi:[0,1]
	v_fmac_f32_e32 v95, v35, v35
	v_pk_mul_f32 v[88:89], v[138:139], v[138:139]
	s_nop 0
	v_add_f32_e32 v35, v88, v95
	v_add_f32_e32 v35, v89, v35
	v_pk_add_f32 v[40:41], v[40:41], v[34:35] op_sel_hi:[1,0] neg_lo:[0,1] neg_hi:[0,1]
	s_nop 0
	v_pk_mul_f32 v[88:89], v[40:41], v[40:41]
	s_nop 0
	v_add_f32_e32 v35, v88, v35
	v_add_f32_e32 v35, v89, v35
	v_pk_add_f32 v[140:141], v[90:91], v[34:35] op_sel_hi:[1,0] neg_lo:[0,1] neg_hi:[0,1]
	s_nop 0
	v_pk_mul_f32 v[88:89], v[140:141], v[140:141]
	s_nop 0
	v_add_f32_e32 v35, v88, v35
	v_add_f32_e32 v35, v89, v35
	v_pk_add_f32 v[142:143], v[92:93], v[34:35] op_sel_hi:[1,0] neg_lo:[0,1] neg_hi:[0,1]
	ds_read_b128 v[92:95], v150 offset:19648
	v_pk_mul_f32 v[88:89], v[142:143], v[142:143]
	s_nop 0
	v_add_f32_e32 v35, v88, v35
	v_add_f32_e32 v35, v89, v35
	ds_bpermute_b32 v104, v149, v35
	ds_read_b128 v[88:91], v150 offset:19584
	s_waitcnt lgkmcnt(1)
	v_add_f32_e32 v35, v35, v104
	ds_bpermute_b32 v104, v148, v35
	s_waitcnt lgkmcnt(0)
	v_add_f32_e32 v35, v35, v104
	v_fmac_f32_e32 v106, 0x3c000000, v35
	v_mul_f32_e32 v35, 0x4b800000, v106
	v_cmp_gt_f32_e32 vcc, s1, v106
	s_nop 1
	v_cndmask_b32_e32 v35, v106, v35, vcc
	v_rsq_f32_e32 v35, v35
	ds_read_b128 v[104:107], v150 offset:19840
	v_mul_f32_e32 v132, 0x45800000, v35
	v_cndmask_b32_e32 v132, v35, v132, vcc
	v_pk_add_f32 v[78:79], v[78:79], v[34:35] op_sel_hi:[1,0] neg_lo:[0,1] neg_hi:[0,1]
	v_cmp_lt_i32_e32 vcc, -1, v68
	v_pk_mul_f32 v[78:79], v[132:133], v[78:79] op_sel_hi:[0,1]
	v_pk_fma_f32 v[36:37], v[36:37], v[78:79], v[62:63]
	v_pk_add_f32 v[62:63], v[76:77], v[34:35] op_sel_hi:[1,0] neg_lo:[0,1] neg_hi:[0,1]
	s_nop 0
	v_pk_mul_f32 v[62:63], v[132:133], v[62:63] op_sel_hi:[0,1]
	v_pk_fma_f32 v[38:39], v[38:39], v[62:63], v[64:65]
	ds_write_b128 v57, v[36:39]
	v_pk_add_f32 v[36:37], v[74:75], v[34:35] op_sel_hi:[1,0] neg_lo:[0,1] neg_hi:[0,1]
	v_pk_add_f32 v[38:39], v[72:73], v[34:35] op_sel_hi:[1,0] neg_lo:[0,1] neg_hi:[0,1]
	v_pk_mul_f32 v[36:37], v[132:133], v[36:37] op_sel_hi:[0,1]
	v_pk_mul_f32 v[38:39], v[132:133], v[38:39] op_sel_hi:[0,1]
	v_pk_fma_f32 v[36:37], v[58:59], v[36:37], v[84:85]
	v_pk_fma_f32 v[38:39], v[60:61], v[38:39], v[86:87]
	ds_write_b128 v57, v[36:39] offset:64
	v_pk_add_f32 v[36:37], v[70:71], v[34:35] op_sel_hi:[1,0] neg_lo:[0,1] neg_hi:[0,1]
	v_pk_add_f32 v[38:39], v[54:55], v[34:35] op_sel_hi:[1,0] neg_lo:[0,1] neg_hi:[0,1]
	v_pk_mul_f32 v[36:37], v[132:133], v[36:37] op_sel_hi:[0,1]
	v_pk_mul_f32 v[38:39], v[132:133], v[38:39] op_sel_hi:[0,1]
	v_pk_fma_f32 v[36:37], v[88:89], v[36:37], v[96:97]
	v_pk_fma_f32 v[38:39], v[90:91], v[38:39], v[98:99]
	ds_write_b128 v57, v[36:39] offset:128
	v_pk_add_f32 v[36:37], v[52:53], v[34:35] op_sel_hi:[1,0] neg_lo:[0,1] neg_hi:[0,1]
	v_pk_add_f32 v[38:39], v[50:51], v[34:35] op_sel_hi:[1,0] neg_lo:[0,1] neg_hi:[0,1]
	v_pk_mul_f32 v[36:37], v[132:133], v[36:37] op_sel_hi:[0,1]
	v_pk_mul_f32 v[38:39], v[132:133], v[38:39] op_sel_hi:[0,1]
	v_pk_fma_f32 v[36:37], v[92:93], v[36:37], v[100:101]
	v_pk_fma_f32 v[38:39], v[94:95], v[38:39], v[102:103]
	ds_write_b128 v57, v[36:39] offset:192
	v_pk_add_f32 v[36:37], v[48:49], v[34:35] op_sel_hi:[1,0] neg_lo:[0,1] neg_hi:[0,1]
	v_pk_add_f32 v[38:39], v[46:47], v[34:35] op_sel_hi:[1,0] neg_lo:[0,1] neg_hi:[0,1]
	v_pk_mul_f32 v[36:37], v[132:133], v[36:37] op_sel_hi:[0,1]
	v_pk_mul_f32 v[38:39], v[132:133], v[38:39] op_sel_hi:[0,1]
	v_pk_fma_f32 v[36:37], v[108:109], v[36:37], v[116:117]
	v_pk_fma_f32 v[38:39], v[110:111], v[38:39], v[118:119]
	ds_write_b128 v57, v[36:39] offset:256
	v_pk_add_f32 v[36:37], v[42:43], v[34:35] op_sel_hi:[1,0] neg_lo:[0,1] neg_hi:[0,1]
	v_pk_add_f32 v[34:35], v[44:45], v[34:35] op_sel_hi:[1,0] neg_lo:[0,1] neg_hi:[0,1]
	v_pk_mul_f32 v[36:37], v[132:133], v[36:37] op_sel_hi:[0,1]
	v_pk_mul_f32 v[34:35], v[132:133], v[34:35] op_sel_hi:[0,1]
	v_pk_fma_f32 v[36:37], v[112:113], v[36:37], v[120:121]
	v_pk_fma_f32 v[38:39], v[114:115], v[34:35], v[122:123]
	ds_write_b128 v57, v[36:39] offset:320
	v_pk_mul_f32 v[34:35], v[132:133], v[138:139] op_sel_hi:[0,1]
	v_pk_mul_f32 v[36:37], v[132:133], v[40:41] op_sel_hi:[0,1]
	s_waitcnt lgkmcnt(6)
	v_pk_fma_f32 v[34:35], v[104:105], v[34:35], v[128:129]
	v_pk_fma_f32 v[36:37], v[106:107], v[36:37], v[130:131]
	ds_write_b128 v57, v[34:37] offset:384
	v_pk_mul_f32 v[34:35], v[132:133], v[140:141] op_sel_hi:[0,1]
	v_pk_mul_f32 v[36:37], v[132:133], v[142:143] op_sel_hi:[0,1]
	v_pk_fma_f32 v[34:35], v[124:125], v[34:35], v[134:135]
	v_pk_fma_f32 v[36:37], v[126:127], v[36:37], v[136:137]
	v_add_u32_e32 v50, v83, v69
	ds_write_b128 v57, v[34:37] offset:448
	ds_read_b32 v84, v56 offset:8
	ds_read_b32 v85, v56 offset:16
	ds_read_b32 v86, v56 offset:24
	ds_read_b32 v87, v56 offset:32
	ds_read_b32 v88, v56 offset:40
	ds_read_b32 v89, v56 offset:48
	ds_read_b32 v90, v56 offset:56
	ds_read_b128 v[100:103], v50
	ds_read_b128 v[104:107], v81
	ds_read_b128 v[108:111], v80
	ds_read_b128 v[112:115], v80 offset:1088
	ds_read_b128 v[116:119], v80 offset:2176
	ds_read_b128 v[120:123], v80 offset:3264
	ds_read_b128 v[124:127], v80 offset:4352
	ds_read_b128 v[128:131], v80 offset:5440
	v_or_b32_e32 v51, 0x4400, v150
	s_mov_b32 s1, s0
	v_mov_b32_e32 v97, 0
	v_cmp_lt_i32_e32 vcc, -1, v68
	v_lshlrev_b32_e32 v96, 9, v68
	v_lshl_add_u64 v[92:93], v[0:1], 0, v[96:97]
	s_waitcnt lgkmcnt(7)
	s_and_saveexec_b64 s[2:3], vcc
	global_store_dwordx4 v[92:93], v[100:103], off nt
	s_mov_b64 exec, s[2:3]
	v_cmp_lt_i32_e32 vcc, -1, v84
	v_lshlrev_b32_e32 v96, 9, v84
	v_lshl_add_u64 v[94:95], v[0:1], 0, v[96:97]
	s_waitcnt lgkmcnt(6)
	s_and_saveexec_b64 s[2:3], vcc
	global_store_dwordx4 v[94:95], v[104:107], off nt
	s_mov_b64 exec, s[2:3]
	v_cmp_lt_i32_e32 vcc, -1, v85
	v_lshlrev_b32_e32 v96, 9, v85
	v_lshl_add_u64 v[92:93], v[0:1], 0, v[96:97]
	s_waitcnt lgkmcnt(5)
	s_and_saveexec_b64 s[2:3], vcc
	global_store_dwordx4 v[92:93], v[108:111], off nt
	s_mov_b64 exec, s[2:3]
	v_cmp_lt_i32_e32 vcc, -1, v86
	v_lshlrev_b32_e32 v96, 9, v86
	v_lshl_add_u64 v[94:95], v[0:1], 0, v[96:97]
	s_waitcnt lgkmcnt(4)
	s_and_saveexec_b64 s[2:3], vcc
	global_store_dwordx4 v[94:95], v[112:115], off nt
	s_mov_b64 exec, s[2:3]
	v_cmp_lt_i32_e32 vcc, -1, v87
	v_lshlrev_b32_e32 v96, 9, v87
	v_lshl_add_u64 v[92:93], v[0:1], 0, v[96:97]
	s_waitcnt lgkmcnt(3)
	s_and_saveexec_b64 s[2:3], vcc
	global_store_dwordx4 v[92:93], v[116:119], off nt
	s_mov_b64 exec, s[2:3]
	v_cmp_lt_i32_e32 vcc, -1, v88
	v_lshlrev_b32_e32 v96, 9, v88
	v_lshl_add_u64 v[94:95], v[0:1], 0, v[96:97]
	s_waitcnt lgkmcnt(2)
	s_and_saveexec_b64 s[2:3], vcc
	global_store_dwordx4 v[94:95], v[120:123], off nt
	s_mov_b64 exec, s[2:3]
	v_cmp_lt_i32_e32 vcc, -1, v89
	v_lshlrev_b32_e32 v96, 9, v89
	v_lshl_add_u64 v[92:93], v[0:1], 0, v[96:97]
	s_waitcnt lgkmcnt(1)
	s_and_saveexec_b64 s[2:3], vcc
	global_store_dwordx4 v[92:93], v[124:127], off nt
	s_mov_b64 exec, s[2:3]
	v_cmp_lt_i32_e32 vcc, -1, v90
	v_lshlrev_b32_e32 v96, 9, v90
	v_lshl_add_u64 v[94:95], v[0:1], 0, v[96:97]
	s_waitcnt lgkmcnt(0)
	s_and_saveexec_b64 s[2:3], vcc
	global_store_dwordx4 v[94:95], v[128:131], off nt
	s_mov_b64 exec, s[2:3]
